# speedup vs baseline: 1.0270x; 1.0118x over previous
.LBB1_14:
	v_add_u32_e32 v118, s4, v224
	ds_read_b128 v[66:69], v118
	ds_read_b128 v[98:101], v218 offset:8192
	ds_read_b128 v[102:105], v118 offset:32
	ds_read_b128 v[82:85], v118 offset:384
	ds_read_b128 v[86:89], v118 offset:416
	ds_read_b128 v[90:93], v118 offset:448
	ds_read_b128 v[94:97], v118 offset:480
	s_waitcnt lgkmcnt(6)
	v_pk_add_f16 v66, v142, v66
	v_pk_add_f16 v67, v143, v67
	v_pk_add_f16 v68, v144, v68
	v_pk_add_f16 v69, v145, v69
	v_or_b32_e32 v71, 0x80008000, v68
	v_or_b32_e32 v70, 0x80008000, v69
	v_or_b32_e32 v72, 0x80008000, v67
	v_or_b32_e32 v73, 0x80008000, v66
	v_pk_fma_f16 v74, v73, s3, v221 op_sel_hi:[1,0,0]
	v_pk_fma_f16 v75, v72, s3, v221 op_sel_hi:[1,0,0]
	v_pk_fma_f16 v76, v71, s3, v221 op_sel_hi:[1,0,0]
	v_pk_fma_f16 v77, v70, s3, v221 op_sel_hi:[1,0,0]
	v_pk_fma_f16 v76, v76, v71, s20 op_sel_hi:[1,1,0]
	v_pk_fma_f16 v77, v77, v70, s20 op_sel_hi:[1,1,0]
	v_pk_fma_f16 v75, v75, v72, s20 op_sel_hi:[1,1,0]
	v_pk_fma_f16 v74, v74, v73, s20 op_sel_hi:[1,1,0]
	v_pk_fma_f16 v75, v75, v72, s21 op_sel_hi:[1,1,0]
	v_pk_fma_f16 v74, v74, v73, s21 op_sel_hi:[1,1,0]
	v_pk_fma_f16 v76, v76, v71, s21 op_sel_hi:[1,1,0]
	v_pk_fma_f16 v77, v77, v70, s21 op_sel_hi:[1,1,0]
	v_pk_max_f16 v66, v66, 0
	v_exp_f16_e32 v78, v74
	v_exp_f16_e32 v79, v75
	v_exp_f16_e32 v80, v76
	v_exp_f16_e32 v81, v77
	v_exp_f16_sdwa v78, v74 dst_sel:WORD_1 dst_unused:UNUSED_PRESERVE src0_sel:WORD_1
	v_exp_f16_sdwa v79, v75 dst_sel:WORD_1 dst_unused:UNUSED_PRESERVE src0_sel:WORD_1
	v_exp_f16_sdwa v80, v76 dst_sel:WORD_1 dst_unused:UNUSED_PRESERVE src0_sel:WORD_1
	v_exp_f16_sdwa v81, v77 dst_sel:WORD_1 dst_unused:UNUSED_PRESERVE src0_sel:WORD_1
	v_pk_max_f16 v67, v67, 0
	v_pk_max_f16 v68, v68, 0
	v_pk_max_f16 v69, v69, 0
	v_pk_fma_f16 v108, v71, v80, v68
	v_pk_fma_f16 v109, v70, v81, v69
	v_pk_fma_f16 v107, v72, v79, v67
	v_pk_fma_f16 v106, v73, v78, v66
	ds_read_b128 v[66:69], v118 offset:512
	ds_read_b128 v[70:73], v118 offset:544
	ds_read_b128 v[74:77], v118 offset:576
	ds_read_b128 v[78:81], v118 offset:608
	ds_read_b128 v[110:113], v218 offset:9216
	s_waitcnt lgkmcnt(5)
	v_mfma_f32_32x32x16_f16 v[82:97], v[150:153], v[106:109], v[82:97]
	s_waitcnt lgkmcnt(1)
	v_mfma_f32_32x32x16_f16 v[66:81], v[98:101], v[106:109], v[66:81]
	v_pk_add_f16 v98, v146, v102
	v_pk_add_f16 v99, v147, v103
	v_pk_add_f16 v100, v148, v104
	v_pk_add_f16 v101, v149, v105
	v_or_b32_e32 v103, 0x80008000, v100
	v_or_b32_e32 v102, 0x80008000, v101
	v_or_b32_e32 v104, 0x80008000, v99
	v_or_b32_e32 v105, 0x80008000, v98
	v_pk_fma_f16 v106, v105, s3, v221 op_sel_hi:[1,0,0]
	v_pk_fma_f16 v107, v104, s3, v221 op_sel_hi:[1,0,0]
	v_pk_fma_f16 v108, v103, s3, v221 op_sel_hi:[1,0,0]
	v_pk_fma_f16 v109, v102, s3, v221 op_sel_hi:[1,0,0]
	v_pk_fma_f16 v108, v108, v103, s20 op_sel_hi:[1,1,0]
	v_pk_fma_f16 v109, v109, v102, s20 op_sel_hi:[1,1,0]
	v_pk_fma_f16 v107, v107, v104, s20 op_sel_hi:[1,1,0]
	v_pk_fma_f16 v106, v106, v105, s20 op_sel_hi:[1,1,0]
	v_pk_fma_f16 v107, v107, v104, s21 op_sel_hi:[1,1,0]
	v_pk_fma_f16 v106, v106, v105, s21 op_sel_hi:[1,1,0]
	v_pk_fma_f16 v108, v108, v103, s21 op_sel_hi:[1,1,0]
	v_pk_fma_f16 v109, v109, v102, s21 op_sel_hi:[1,1,0]
	v_pk_max_f16 v98, v98, 0
	v_pk_max_f16 v99, v99, 0
	v_pk_max_f16 v100, v100, 0
	v_pk_max_f16 v101, v101, 0
	v_exp_f16_e32 v114, v106
	v_exp_f16_e32 v115, v107
	v_exp_f16_e32 v116, v108
	v_exp_f16_e32 v117, v109
	v_exp_f16_sdwa v114, v106 dst_sel:WORD_1 dst_unused:UNUSED_PRESERVE src0_sel:WORD_1
	v_exp_f16_sdwa v115, v107 dst_sel:WORD_1 dst_unused:UNUSED_PRESERVE src0_sel:WORD_1
	v_exp_f16_sdwa v116, v108 dst_sel:WORD_1 dst_unused:UNUSED_PRESERVE src0_sel:WORD_1
	v_exp_f16_sdwa v117, v109 dst_sel:WORD_1 dst_unused:UNUSED_PRESERVE src0_sel:WORD_1
	s_nop 0
	v_pk_fma_f16 v101, v102, v117, v101
	v_pk_fma_f16 v100, v103, v116, v100
	v_pk_fma_f16 v99, v104, v115, v99
	v_pk_fma_f16 v98, v105, v114, v98
	ds_read_b128 v[102:105], v118 offset:64
	ds_read_b128 v[106:109], v218 offset:2048
	v_mfma_f32_32x32x16_f16 v[82:97], v[154:157], v[98:101], v[82:97]
	v_add_u32_e32 v225, s4, v223
	ds_read_b128 v[126:129], v225
	ds_read_b128 v[130:133], v225 offset:16
	ds_read_b128 v[134:137], v225 offset:32
	ds_read_b128 v[138:141], v225 offset:48
	ds_read_b128 v[150:153], v218 offset:19456
	ds_read_b128 v[154:157], v218 offset:20480
	s_waitcnt lgkmcnt(7)
	v_pk_add_f16 v102, v158, v102
	v_pk_add_f16 v103, v159, v103
	v_pk_add_f16 v104, v160, v104
	v_pk_add_f16 v105, v161, v105
	v_mfma_f32_32x32x16_f16 v[66:81], v[110:113], v[98:101], v[66:81]
	v_or_b32_e32 v110, 0x80008000, v105
	v_or_b32_e32 v111, 0x80008000, v104
	v_or_b32_e32 v112, 0x80008000, v103
	v_or_b32_e32 v113, 0x80008000, v102
	v_pk_fma_f16 v114, v113, s3, v221 op_sel_hi:[1,0,0]
	v_pk_fma_f16 v115, v112, s3, v221 op_sel_hi:[1,0,0]
	v_pk_fma_f16 v116, v111, s3, v221 op_sel_hi:[1,0,0]
	v_pk_fma_f16 v117, v110, s3, v221 op_sel_hi:[1,0,0]
	ds_read_b128 v[98:101], v118 offset:96
	v_pk_fma_f16 v117, v117, v110, s20 op_sel_hi:[1,1,0]
	v_pk_fma_f16 v116, v116, v111, s20 op_sel_hi:[1,1,0]
	v_pk_fma_f16 v115, v115, v112, s20 op_sel_hi:[1,1,0]
	v_pk_fma_f16 v114, v114, v113, s20 op_sel_hi:[1,1,0]
	v_pk_max_f16 v102, v102, 0
	v_pk_max_f16 v103, v103, 0
	v_pk_max_f16 v104, v104, 0
	v_pk_max_f16 v105, v105, 0
	v_pk_fma_f16 v114, v114, v113, s21 op_sel_hi:[1,1,0]
	v_pk_fma_f16 v115, v115, v112, s21 op_sel_hi:[1,1,0]
	v_pk_fma_f16 v116, v116, v111, s21 op_sel_hi:[1,1,0]
	v_pk_fma_f16 v117, v117, v110, s21 op_sel_hi:[1,1,0]
	s_nop 0
	v_exp_f16_e32 v119, v114
	v_exp_f16_e32 v120, v115
	v_exp_f16_e32 v121, v116
	v_exp_f16_e32 v122, v117
	v_exp_f16_sdwa v119, v114 dst_sel:WORD_1 dst_unused:UNUSED_PRESERVE src0_sel:WORD_1
	v_exp_f16_sdwa v120, v115 dst_sel:WORD_1 dst_unused:UNUSED_PRESERVE src0_sel:WORD_1
	v_exp_f16_sdwa v121, v116 dst_sel:WORD_1 dst_unused:UNUSED_PRESERVE src0_sel:WORD_1
	v_exp_f16_sdwa v122, v117 dst_sel:WORD_1 dst_unused:UNUSED_PRESERVE src0_sel:WORD_1
	s_nop 0
	v_pk_fma_f16 v105, v110, v122, v105
	v_pk_fma_f16 v104, v111, v121, v104
	v_pk_fma_f16 v103, v112, v120, v103
	v_pk_fma_f16 v102, v113, v119, v102
	ds_read_b128 v[110:113], v218 offset:3072
	s_waitcnt lgkmcnt(1)
	v_pk_add_f16 v98, v162, v98
	v_mfma_f32_32x32x16_f16 v[82:97], v[106:109], v[102:105], v[82:97]
	ds_read_b128 v[106:109], v218 offset:10240
	ds_read_b128 v[114:117], v218 offset:11264
	v_pk_add_f16 v99, v163, v99
	v_pk_add_f16 v100, v164, v100
	v_pk_add_f16 v101, v165, v101
	s_waitcnt lgkmcnt(1)
	v_mfma_f32_32x32x16_f16 v[66:81], v[106:109], v[102:105], v[66:81]
	s_setprio 0
	v_or_b32_e32 v102, 0x80008000, v101
	v_or_b32_e32 v103, 0x80008000, v100
	v_or_b32_e32 v104, 0x80008000, v99
	v_or_b32_e32 v105, 0x80008000, v98
	v_pk_fma_f16 v106, v105, s3, v221 op_sel_hi:[1,0,0]
	v_pk_fma_f16 v107, v104, s3, v221 op_sel_hi:[1,0,0]
	v_pk_fma_f16 v108, v103, s3, v221 op_sel_hi:[1,0,0]
	v_pk_fma_f16 v109, v102, s3, v221 op_sel_hi:[1,0,0]
	v_pk_fma_f16 v108, v108, v103, s20 op_sel_hi:[1,1,0]
	v_pk_fma_f16 v109, v109, v102, s20 op_sel_hi:[1,1,0]
	v_pk_fma_f16 v107, v107, v104, s20 op_sel_hi:[1,1,0]
	v_pk_fma_f16 v106, v106, v105, s20 op_sel_hi:[1,1,0]
	v_pk_fma_f16 v107, v107, v104, s21 op_sel_hi:[1,1,0]
	v_pk_fma_f16 v106, v106, v105, s21 op_sel_hi:[1,1,0]
	v_pk_fma_f16 v108, v108, v103, s21 op_sel_hi:[1,1,0]
	v_pk_fma_f16 v109, v109, v102, s21 op_sel_hi:[1,1,0]
	v_pk_max_f16 v98, v98, 0
	v_pk_max_f16 v99, v99, 0
	v_pk_max_f16 v100, v100, 0
	v_pk_max_f16 v101, v101, 0
	v_exp_f16_e32 v119, v106
	v_exp_f16_e32 v120, v107
	v_exp_f16_e32 v121, v108
	v_exp_f16_e32 v122, v109
	v_exp_f16_sdwa v119, v106 dst_sel:WORD_1 dst_unused:UNUSED_PRESERVE src0_sel:WORD_1
	v_exp_f16_sdwa v120, v107 dst_sel:WORD_1 dst_unused:UNUSED_PRESERVE src0_sel:WORD_1
	v_exp_f16_sdwa v121, v108 dst_sel:WORD_1 dst_unused:UNUSED_PRESERVE src0_sel:WORD_1
	v_exp_f16_sdwa v122, v109 dst_sel:WORD_1 dst_unused:UNUSED_PRESERVE src0_sel:WORD_1
	s_nop 0
	v_pk_fma_f16 v101, v102, v122, v101
	v_pk_fma_f16 v100, v103, v121, v100
	v_pk_fma_f16 v99, v104, v120, v99
	v_pk_fma_f16 v98, v105, v119, v98
	ds_read_b128 v[102:105], v118 offset:128
	ds_read_b128 v[106:109], v218 offset:4096
	v_mfma_f32_32x32x16_f16 v[82:97], v[110:113], v[98:101], v[82:97]
	s_waitcnt lgkmcnt(1)
	v_pk_add_f16 v102, v166, v102
	v_pk_add_f16 v103, v167, v103
	v_pk_add_f16 v104, v168, v104
	v_pk_add_f16 v105, v169, v105
	v_or_b32_e32 v111, 0x80008000, v104
	v_mfma_f32_32x32x16_f16 v[66:81], v[114:117], v[98:101], v[66:81]
	ds_read_b128 v[226:229], v222
	ds_read_b128 v[230:233], v222 offset:1024
	ds_read_b128 v[234:237], v222 offset:2048
	ds_read_b128 v[238:241], v222 offset:3072
	v_or_b32_e32 v110, 0x80008000, v105
	v_or_b32_e32 v112, 0x80008000, v103
	v_or_b32_e32 v113, 0x80008000, v102
	v_pk_fma_f16 v114, v113, s3, v221 op_sel_hi:[1,0,0]
	v_pk_fma_f16 v115, v112, s3, v221 op_sel_hi:[1,0,0]
	v_pk_fma_f16 v116, v111, s3, v221 op_sel_hi:[1,0,0]
	v_pk_fma_f16 v117, v110, s3, v221 op_sel_hi:[1,0,0]
	ds_read_b128 v[98:101], v118 offset:160
	v_pk_fma_f16 v117, v117, v110, s20 op_sel_hi:[1,1,0]
	v_pk_fma_f16 v116, v116, v111, s20 op_sel_hi:[1,1,0]
	v_pk_fma_f16 v115, v115, v112, s20 op_sel_hi:[1,1,0]
	v_pk_fma_f16 v114, v114, v113, s20 op_sel_hi:[1,1,0]
	v_pk_max_f16 v102, v102, 0
	v_pk_max_f16 v103, v103, 0
	v_pk_max_f16 v104, v104, 0
	v_pk_max_f16 v105, v105, 0
	v_pk_fma_f16 v114, v114, v113, s21 op_sel_hi:[1,1,0]
	v_pk_fma_f16 v115, v115, v112, s21 op_sel_hi:[1,1,0]
	v_pk_fma_f16 v116, v116, v111, s21 op_sel_hi:[1,1,0]
	v_pk_fma_f16 v117, v117, v110, s21 op_sel_hi:[1,1,0]
	s_nop 0
	v_exp_f16_e32 v119, v114
	v_exp_f16_e32 v120, v115
	v_exp_f16_e32 v121, v116
	v_exp_f16_e32 v122, v117
	v_exp_f16_sdwa v119, v114 dst_sel:WORD_1 dst_unused:UNUSED_PRESERVE src0_sel:WORD_1
	v_exp_f16_sdwa v120, v115 dst_sel:WORD_1 dst_unused:UNUSED_PRESERVE src0_sel:WORD_1
	v_exp_f16_sdwa v121, v116 dst_sel:WORD_1 dst_unused:UNUSED_PRESERVE src0_sel:WORD_1
	v_exp_f16_sdwa v122, v117 dst_sel:WORD_1 dst_unused:UNUSED_PRESERVE src0_sel:WORD_1
	s_nop 0
	v_pk_fma_f16 v105, v110, v122, v105
	v_pk_fma_f16 v104, v111, v121, v104
	v_pk_fma_f16 v103, v112, v120, v103
	v_pk_fma_f16 v102, v113, v119, v102
	ds_read_b128 v[110:113], v218 offset:5120
	s_waitcnt lgkmcnt(1)
	v_pk_add_f16 v98, v170, v98
	v_mfma_f32_32x32x16_f16 v[82:97], v[106:109], v[102:105], v[82:97]
	ds_read_b128 v[106:109], v218 offset:12288
	ds_read_b128 v[114:117], v218 offset:13312
	v_pk_add_f16 v99, v171, v99
	v_pk_add_f16 v100, v172, v100
	v_pk_add_f16 v101, v173, v101
	s_waitcnt lgkmcnt(1)
	v_mfma_f32_32x32x16_f16 v[66:81], v[106:109], v[102:105], v[66:81]
	v_or_b32_e32 v102, 0x80008000, v101
	v_or_b32_e32 v103, 0x80008000, v100
	v_or_b32_e32 v104, 0x80008000, v99
	v_or_b32_e32 v105, 0x80008000, v98
	v_pk_fma_f16 v106, v105, s3, v221 op_sel_hi:[1,0,0]
	v_pk_fma_f16 v107, v104, s3, v221 op_sel_hi:[1,0,0]
	v_pk_fma_f16 v108, v103, s3, v221 op_sel_hi:[1,0,0]
	v_pk_fma_f16 v109, v102, s3, v221 op_sel_hi:[1,0,0]
	v_pk_fma_f16 v108, v108, v103, s20 op_sel_hi:[1,1,0]
	v_pk_fma_f16 v109, v109, v102, s20 op_sel_hi:[1,1,0]
	v_pk_fma_f16 v107, v107, v104, s20 op_sel_hi:[1,1,0]
	v_pk_fma_f16 v106, v106, v105, s20 op_sel_hi:[1,1,0]
	v_pk_fma_f16 v107, v107, v104, s21 op_sel_hi:[1,1,0]
	v_pk_fma_f16 v106, v106, v105, s21 op_sel_hi:[1,1,0]
	v_pk_fma_f16 v108, v108, v103, s21 op_sel_hi:[1,1,0]
	v_pk_fma_f16 v109, v109, v102, s21 op_sel_hi:[1,1,0]
	v_pk_max_f16 v98, v98, 0
	v_pk_max_f16 v99, v99, 0
	v_pk_max_f16 v100, v100, 0
	v_pk_max_f16 v101, v101, 0
	v_exp_f16_e32 v119, v106
	v_exp_f16_e32 v120, v107
	v_exp_f16_e32 v121, v108
	v_exp_f16_e32 v122, v109
	v_exp_f16_sdwa v119, v106 dst_sel:WORD_1 dst_unused:UNUSED_PRESERVE src0_sel:WORD_1
	v_exp_f16_sdwa v120, v107 dst_sel:WORD_1 dst_unused:UNUSED_PRESERVE src0_sel:WORD_1
	v_exp_f16_sdwa v121, v108 dst_sel:WORD_1 dst_unused:UNUSED_PRESERVE src0_sel:WORD_1
	v_exp_f16_sdwa v122, v109 dst_sel:WORD_1 dst_unused:UNUSED_PRESERVE src0_sel:WORD_1
	s_nop 0
	v_pk_fma_f16 v101, v102, v122, v101
	v_pk_fma_f16 v100, v103, v121, v100
	v_pk_fma_f16 v99, v104, v120, v99
	v_pk_fma_f16 v98, v105, v119, v98
	ds_read_b128 v[102:105], v118 offset:192
	ds_read_b128 v[106:109], v218 offset:6144
	v_mfma_f32_32x32x16_f16 v[82:97], v[110:113], v[98:101], v[82:97]
	s_waitcnt lgkmcnt(1)
	v_pk_add_f16 v102, v174, v102
	v_pk_add_f16 v103, v175, v103
	v_pk_add_f16 v104, v176, v104
	v_pk_add_f16 v105, v177, v105
	v_or_b32_e32 v111, 0x80008000, v104
	v_mfma_f32_32x32x16_f16 v[66:81], v[114:117], v[98:101], v[66:81]
	v_or_b32_e32 v110, 0x80008000, v105
	v_or_b32_e32 v112, 0x80008000, v103
	v_or_b32_e32 v113, 0x80008000, v102
	v_pk_fma_f16 v114, v113, s3, v221 op_sel_hi:[1,0,0]
	v_pk_fma_f16 v115, v112, s3, v221 op_sel_hi:[1,0,0]
	v_pk_fma_f16 v116, v111, s3, v221 op_sel_hi:[1,0,0]
	v_pk_fma_f16 v117, v110, s3, v221 op_sel_hi:[1,0,0]
	ds_read_b128 v[98:101], v118 offset:224
	v_pk_fma_f16 v117, v117, v110, s20 op_sel_hi:[1,1,0]
	v_pk_fma_f16 v116, v116, v111, s20 op_sel_hi:[1,1,0]
	v_pk_fma_f16 v115, v115, v112, s20 op_sel_hi:[1,1,0]
	v_pk_fma_f16 v114, v114, v113, s20 op_sel_hi:[1,1,0]
	v_pk_max_f16 v102, v102, 0
	v_pk_max_f16 v103, v103, 0
	v_pk_max_f16 v104, v104, 0
	v_pk_max_f16 v105, v105, 0
	v_pk_fma_f16 v114, v114, v113, s21 op_sel_hi:[1,1,0]
	v_pk_fma_f16 v115, v115, v112, s21 op_sel_hi:[1,1,0]
	v_pk_fma_f16 v116, v116, v111, s21 op_sel_hi:[1,1,0]
	v_pk_fma_f16 v117, v117, v110, s21 op_sel_hi:[1,1,0]
	s_waitcnt lgkmcnt(0)
	v_pk_add_f16 v98, v178, v98
	ds_read_b128 v[242:245], v218 offset:16384
	ds_read_b128 v[246:249], v218 offset:17408
	ds_read_b128 v[250:253], v218 offset:18432
	v_exp_f16_e32 v118, v114
	v_exp_f16_e32 v119, v115
	v_exp_f16_e32 v120, v116
	v_exp_f16_e32 v121, v117
	v_exp_f16_sdwa v118, v114 dst_sel:WORD_1 dst_unused:UNUSED_PRESERVE src0_sel:WORD_1
	v_exp_f16_sdwa v119, v115 dst_sel:WORD_1 dst_unused:UNUSED_PRESERVE src0_sel:WORD_1
	v_exp_f16_sdwa v120, v116 dst_sel:WORD_1 dst_unused:UNUSED_PRESERVE src0_sel:WORD_1
	v_exp_f16_sdwa v121, v117 dst_sel:WORD_1 dst_unused:UNUSED_PRESERVE src0_sel:WORD_1
	v_pk_add_f16 v99, v179, v99
	v_pk_fma_f16 v105, v110, v121, v105
	v_pk_fma_f16 v104, v111, v120, v104
	v_pk_fma_f16 v103, v112, v119, v103
	v_pk_fma_f16 v102, v113, v118, v102
	ds_read_b128 v[110:113], v218 offset:7168
	v_pk_add_f16 v100, v180, v100
	v_mfma_f32_32x32x16_f16 v[82:97], v[106:109], v[102:105], v[82:97]
	ds_read_b128 v[106:109], v218 offset:14336
	ds_read_b128 v[114:117], v218 offset:15360
	v_pk_add_f16 v101, v181, v101
	s_waitcnt lgkmcnt(1)
	v_mfma_f32_32x32x16_f16 v[66:81], v[106:109], v[102:105], v[66:81]
	v_or_b32_e32 v102, 0x80008000, v101
	v_or_b32_e32 v103, 0x80008000, v100
	v_or_b32_e32 v104, 0x80008000, v99
	v_or_b32_e32 v105, 0x80008000, v98
	v_pk_fma_f16 v106, v105, s3, v221 op_sel_hi:[1,0,0]
	v_pk_fma_f16 v107, v104, s3, v221 op_sel_hi:[1,0,0]
	v_pk_fma_f16 v108, v103, s3, v221 op_sel_hi:[1,0,0]
	v_pk_fma_f16 v109, v102, s3, v221 op_sel_hi:[1,0,0]
	v_pk_fma_f16 v108, v108, v103, s20 op_sel_hi:[1,1,0]
	v_pk_fma_f16 v109, v109, v102, s20 op_sel_hi:[1,1,0]
	v_pk_fma_f16 v107, v107, v104, s20 op_sel_hi:[1,1,0]
	v_pk_fma_f16 v106, v106, v105, s20 op_sel_hi:[1,1,0]
	v_pk_max_f16 v98, v98, 0
	v_pk_max_f16 v99, v99, 0
	v_pk_max_f16 v100, v100, 0
	v_pk_max_f16 v101, v101, 0
	v_pk_fma_f16 v106, v106, v105, s21 op_sel_hi:[1,1,0]
	v_pk_fma_f16 v107, v107, v104, s21 op_sel_hi:[1,1,0]
	v_pk_fma_f16 v108, v108, v103, s21 op_sel_hi:[1,1,0]
	v_pk_fma_f16 v109, v109, v102, s21 op_sel_hi:[1,1,0]
	s_nop 0
	v_exp_f16_e32 v118, v106
	v_exp_f16_e32 v119, v107
	v_exp_f16_e32 v120, v108
	v_exp_f16_e32 v121, v109
	v_exp_f16_sdwa v118, v106 dst_sel:WORD_1 dst_unused:UNUSED_PRESERVE src0_sel:WORD_1
	v_exp_f16_sdwa v119, v107 dst_sel:WORD_1 dst_unused:UNUSED_PRESERVE src0_sel:WORD_1
	v_exp_f16_sdwa v120, v108 dst_sel:WORD_1 dst_unused:UNUSED_PRESERVE src0_sel:WORD_1
	v_exp_f16_sdwa v121, v109 dst_sel:WORD_1 dst_unused:UNUSED_PRESERVE src0_sel:WORD_1
	s_nop 0
	v_pk_fma_f16 v101, v102, v121, v101
	v_pk_fma_f16 v100, v103, v120, v100
	v_pk_fma_f16 v99, v104, v119, v99
	v_pk_fma_f16 v98, v105, v118, v98
	s_nop 1
	v_mfma_f32_32x32x16_f16 v[82:97], v[110:113], v[98:101], v[82:97]
	s_waitcnt lgkmcnt(0)
	v_mfma_f32_32x32x16_f16 v[66:81], v[114:117], v[98:101], v[66:81]
	s_setprio 2
	ds_read_b128 v[98:101], v222 offset:4096
	ds_read_b128 v[102:105], v222 offset:5120
	ds_read_b128 v[106:109], v222 offset:6144
	ds_read_b128 v[110:113], v222 offset:7168
	s_nop 4
	v_cvt_pk_f16_f32 v114, v82, v83
	v_cvt_pk_f16_f32 v115, v84, v85
	v_cvt_pk_f16_f32 v116, v86, v87
	v_cvt_pk_f16_f32 v117, v88, v89
	v_pk_add_f16 v126, v126, v114
	v_pk_add_f16 v127, v127, v115
	v_pk_add_f16 v128, v128, v116
	v_pk_add_f16 v129, v129, v117
	s_nop 1
	v_mfma_f32_32x32x16_f16 v[226:241], v[242:245], v[126:129], v[226:241]
	ds_read_b128 v[242:245], v218 offset:21504
	v_cvt_pk_f16_f32 v118, v90, v91
	v_cvt_pk_f16_f32 v119, v92, v93
	v_cvt_pk_f16_f32 v120, v94, v95
	v_cvt_pk_f16_f32 v121, v96, v97
	v_pk_add_f16 v130, v130, v118
	v_pk_add_f16 v131, v131, v119
	v_pk_add_f16 v132, v132, v120
	v_pk_add_f16 v133, v133, v121
	s_nop 1
	v_mfma_f32_32x32x16_f16 v[226:241], v[246:249], v[130:133], v[226:241]
	ds_read_b128 v[246:249], v218 offset:22528
	v_cvt_pk_f16_f32 v122, v66, v67
	v_cvt_pk_f16_f32 v123, v68, v69
	v_cvt_pk_f16_f32 v124, v70, v71
	v_cvt_pk_f16_f32 v125, v72, v73
	v_pk_add_f16 v134, v134, v122
	v_pk_add_f16 v135, v135, v123
	v_pk_add_f16 v136, v136, v124
	v_pk_add_f16 v137, v137, v125
	s_nop 1
	v_mfma_f32_32x32x16_f16 v[226:241], v[250:253], v[134:137], v[226:241]
	ds_read_b128 v[250:253], v218 offset:23552
	v_cvt_pk_f16_f32 v182, v74, v75
	v_cvt_pk_f16_f32 v183, v76, v77
	v_cvt_pk_f16_f32 v184, v78, v79
	v_cvt_pk_f16_f32 v185, v80, v81
	v_pk_add_f16 v138, v138, v182
	v_pk_add_f16 v139, v139, v183
	v_pk_add_f16 v140, v140, v184
	v_pk_add_f16 v141, v141, v185
	s_nop 1
	v_mfma_f32_32x32x16_f16 v[226:241], v[150:153], v[138:141], v[226:241]
	ds_read_b128 v[150:153], v218 offset:24576
	ds_read_b128 v[66:69], v222 offset:8192
	ds_read_b128 v[70:73], v222 offset:9216
	ds_read_b128 v[74:77], v222 offset:10240
	ds_read_b128 v[78:81], v222 offset:11264
	ds_read_b128 v[82:85], v222 offset:12288
	ds_read_b128 v[86:89], v222 offset:13312
	ds_read_b128 v[90:93], v222 offset:14336
	ds_read_b128 v[94:97], v222 offset:15360
	s_waitcnt lgkmcnt(12)
	v_mfma_f32_32x32x16_f16 v[98:113], v[154:157], v[126:129], v[98:113]
	ds_read_b128 v[154:157], v218 offset:25600
	s_waitcnt lgkmcnt(12)
	v_mfma_f32_32x32x16_f16 v[98:113], v[242:245], v[130:133], v[98:113]
	ds_read_b128 v[242:245], v218 offset:26624
	s_waitcnt lgkmcnt(12)
	v_mfma_f32_32x32x16_f16 v[98:113], v[246:249], v[134:137], v[98:113]
	ds_read_b128 v[246:249], v218 offset:27648
	v_cvt_pk_f16_f32 v226, v226, v227
	v_cvt_pk_f16_f32 v227, v228, v229
	v_cvt_pk_f16_f32 v228, v230, v231
	v_cvt_pk_f16_f32 v229, v232, v233
	v_pk_max_f16 v226, v226, 0
	v_pk_max_f16 v227, v227, 0
	v_pk_max_f16 v228, v228, 0
	v_pk_max_f16 v229, v229, 0
	s_waitcnt lgkmcnt(12)
	v_mfma_f32_32x32x16_f16 v[98:113], v[250:253], v[138:141], v[98:113]
	ds_read_b128 v[250:253], v218 offset:28672
	v_cvt_pk_f16_f32 v230, v234, v235
	v_cvt_pk_f16_f32 v231, v236, v237
	v_cvt_pk_f16_f32 v232, v238, v239
	v_cvt_pk_f16_f32 v233, v240, v241
	v_pk_max_f16 v230, v230, 0
	v_pk_max_f16 v231, v231, 0
	v_pk_max_f16 v232, v232, 0
	v_pk_max_f16 v233, v233, 0
	s_waitcnt lgkmcnt(8)
	v_mfma_f32_32x32x16_f16 v[66:81], v[150:153], v[126:129], v[66:81]
	ds_read_b128 v[150:153], v218 offset:29696
	s_waitcnt lgkmcnt(4)
	v_mfma_f32_32x32x16_f16 v[66:81], v[154:157], v[130:133], v[66:81]
	ds_read_b128 v[154:157], v218 offset:30720
	s_waitcnt lgkmcnt(4)
	v_mfma_f32_32x32x16_f16 v[66:81], v[242:245], v[134:137], v[66:81]
	ds_read_b128 v[242:245], v218 offset:31744
	v_cvt_pk_f16_f32 v98, v98, v99
	v_cvt_pk_f16_f32 v99, v100, v101
	v_cvt_pk_f16_f32 v100, v102, v103
	v_cvt_pk_f16_f32 v101, v104, v105
	v_pk_max_f16 v98, v98, 0
	v_pk_max_f16 v99, v99, 0
	v_pk_max_f16 v100, v100, 0
	v_pk_max_f16 v101, v101, 0
	s_waitcnt lgkmcnt(4)
	v_mfma_f32_32x32x16_f16 v[66:81], v[246:249], v[138:141], v[66:81]
	ds_read_b128 v[246:249], v218 offset:32768
	v_cvt_pk_f16_f32 v102, v106, v107
	v_cvt_pk_f16_f32 v103, v108, v109
	v_cvt_pk_f16_f32 v104, v110, v111
	v_cvt_pk_f16_f32 v105, v112, v113
	v_pk_max_f16 v102, v102, 0
	v_pk_max_f16 v103, v103, 0
	v_pk_max_f16 v104, v104, 0
	v_pk_max_f16 v105, v105, 0
	s_waitcnt lgkmcnt(4)
	v_mfma_f32_32x32x16_f16 v[82:97], v[250:253], v[126:129], v[82:97]
	ds_read_b128 v[250:253], v218 offset:33792
	s_waitcnt lgkmcnt(4)
	v_mfma_f32_32x32x16_f16 v[82:97], v[150:153], v[130:133], v[82:97]
	ds_read_b128 v[150:153], v218 offset:34816
	s_waitcnt lgkmcnt(4)
	v_mfma_f32_32x32x16_f16 v[82:97], v[154:157], v[134:137], v[82:97]
	ds_read_b128 v[154:157], v218 offset:35840
	v_cvt_pk_f16_f32 v66, v66, v67
	v_cvt_pk_f16_f32 v67, v68, v69
	v_cvt_pk_f16_f32 v68, v70, v71
	v_cvt_pk_f16_f32 v69, v72, v73
	v_pk_max_f16 v66, v66, 0
	v_pk_max_f16 v67, v67, 0
	v_pk_max_f16 v68, v68, 0
	v_pk_max_f16 v69, v69, 0
	s_waitcnt lgkmcnt(4)
	v_mfma_f32_32x32x16_f16 v[82:97], v[242:245], v[138:141], v[82:97]
	ds_read_b128 v[242:245], v218 offset:36864
	v_cvt_pk_f16_f32 v70, v74, v75
	v_cvt_pk_f16_f32 v71, v76, v77
	v_cvt_pk_f16_f32 v72, v78, v79
	v_cvt_pk_f16_f32 v73, v80, v81
	v_pk_max_f16 v70, v70, 0
	v_pk_max_f16 v71, v71, 0
	v_pk_max_f16 v72, v72, 0
	v_pk_max_f16 v73, v73, 0
	s_waitcnt lgkmcnt(4)
	v_mfma_f32_32x32x16_f16 v[126:141], v[246:249], v[226:229], v[2:17]
	ds_read_b128 v[246:249], v218 offset:37888
	s_waitcnt lgkmcnt(4)
	v_mfma_f32_32x32x16_f16 v[126:141], v[250:253], v[230:233], v[126:141]
	ds_read_b128 v[250:253], v218 offset:38912
	s_waitcnt lgkmcnt(4)
	v_mfma_f32_32x32x16_f16 v[126:141], v[150:153], v[98:101], v[126:141]
	ds_read_b128 v[150:153], v218 offset:39936
	s_waitcnt lgkmcnt(4)
	v_mfma_f32_32x32x16_f16 v[126:141], v[154:157], v[102:105], v[126:141]
	ds_read_b128 v[154:157], v218 offset:40960
	s_waitcnt lgkmcnt(4)
	v_mfma_f32_32x32x16_f16 v[126:141], v[242:245], v[66:69], v[126:141]
	ds_read_b128 v[242:245], v218 offset:41984
	v_cvt_pk_f16_f32 v97, v96, v97
	v_cvt_pk_f16_f32 v96, v94, v95
	v_cvt_pk_f16_f32 v95, v92, v93
	v_cvt_pk_f16_f32 v94, v90, v91
	v_pk_max_f16 v97, v97, 0
	v_pk_max_f16 v96, v96, 0
	v_pk_max_f16 v95, v95, 0
	v_pk_max_f16 v94, v94, 0
	s_waitcnt lgkmcnt(4)
	v_mfma_f32_32x32x16_f16 v[126:141], v[246:249], v[70:73], v[126:141]
	ds_read_b128 v[246:249], v218 offset:43008
	v_cvt_pk_f16_f32 v93, v88, v89
	v_cvt_pk_f16_f32 v92, v86, v87
	v_cvt_pk_f16_f32 v91, v84, v85
	v_cvt_pk_f16_f32 v90, v82, v83
	v_pk_max_f16 v93, v93, 0
	v_pk_max_f16 v92, v92, 0
	v_pk_max_f16 v91, v91, 0
	v_pk_max_f16 v90, v90, 0
	s_waitcnt lgkmcnt(4)
	s_nop 0
	v_mfma_f32_32x32x16_f16 v[126:141], v[250:253], v[90:93], v[126:141]
	ds_read_b128 v[250:253], v218 offset:44032
	s_waitcnt lgkmcnt(4)
	v_mfma_f32_32x32x16_f16 v[126:141], v[150:153], v[94:97], v[126:141]
	ds_read_b128 v[150:153], v218 offset:45056
	s_waitcnt lgkmcnt(4)
	v_mfma_f32_32x32x16_f16 v[74:89], v[154:157], v[226:229], v[34:49]
	ds_read_b128 v[154:157], v218 offset:46080
	s_waitcnt lgkmcnt(4)
	v_mfma_f32_32x32x16_f16 v[74:89], v[242:245], v[230:233], v[74:89]
	ds_read_b128 v[242:245], v218 offset:47104
	s_waitcnt lgkmcnt(4)
	v_mfma_f32_32x32x16_f16 v[74:89], v[246:249], v[98:101], v[74:89]
	ds_read_b128 v[246:249], v218 offset:48128
	s_waitcnt lgkmcnt(4)
	v_mfma_f32_32x32x16_f16 v[74:89], v[250:253], v[102:105], v[74:89]
	s_waitcnt lgkmcnt(3)
	v_mfma_f32_32x32x16_f16 v[74:89], v[150:153], v[66:69], v[74:89]
	ds_read_b128 v[150:153], v218
	v_max3_f32 v254, v126, v127, v128
	v_max3_f32 v255, v129, v130, v131
	v_max3_f32 v254, v254, v132, v133
	v_max3_f32 v255, v255, v134, v135
	v_max3_f32 v254, v254, v136, v137
	v_max3_f32 v255, v255, v138, v139
	v_max3_f32 v254, v254, v140, v141
	v_max_f32_e32 v254, v254, v255
	v_cmp_lt_f32_e32 vcc, s5, v254
	s_cbranch_vccz .Lm_norescale0
	v_max_f32_e32 v234, 0, v126
	v_max_f32_e32 v235, 0, v127
	v_max_f32_e32 v236, 0, v128
	v_max_f32_e32 v237, 0, v129
	v_max_f32_e32 v238, 0, v130
	v_max_f32_e32 v239, 0, v131
	v_max_f32_e32 v240, 0, v132
	v_max_f32_e32 v241, 0, v133
	v_max_f32_e32 v106, 0, v134
	v_max_f32_e32 v107, 0, v135
	v_max_f32_e32 v108, 0, v136
	v_max_f32_e32 v109, 0, v137
	v_max_f32_e32 v110, 0, v138
	v_max_f32_e32 v111, 0, v139
	v_max_f32_e32 v112, 0, v140
	v_max_f32_e32 v113, 0, v141
	v_sub_f32_e32 v126, v126, v234
	v_sub_f32_e32 v127, v127, v235
	v_sub_f32_e32 v128, v128, v236
	v_sub_f32_e32 v129, v129, v237
	v_sub_f32_e32 v130, v130, v238
	v_sub_f32_e32 v131, v131, v239
	v_sub_f32_e32 v132, v132, v240
	v_sub_f32_e32 v133, v133, v241
	v_sub_f32_e32 v134, v134, v106
	v_sub_f32_e32 v135, v135, v107
	v_sub_f32_e32 v136, v136, v108
	v_sub_f32_e32 v137, v137, v109
	v_sub_f32_e32 v138, v138, v110
	v_sub_f32_e32 v139, v139, v111
	v_sub_f32_e32 v140, v140, v112
	v_sub_f32_e32 v141, v141, v113
	v_sub_f32_e32 v2, v2, v234
	v_sub_f32_e32 v3, v3, v235
	v_sub_f32_e32 v4, v4, v236
	v_sub_f32_e32 v5, v5, v237
	v_sub_f32_e32 v6, v6, v238
	v_sub_f32_e32 v7, v7, v239
	v_sub_f32_e32 v8, v8, v240
	v_sub_f32_e32 v9, v9, v241
	v_sub_f32_e32 v10, v10, v106
	v_sub_f32_e32 v11, v11, v107
	v_sub_f32_e32 v12, v12, v108
	v_sub_f32_e32 v13, v13, v109
	v_sub_f32_e32 v14, v14, v110
	v_sub_f32_e32 v15, v15, v111
	v_sub_f32_e32 v16, v16, v112
	v_sub_f32_e32 v17, v17, v113
	v_exp_f32_e64 v234, -v234
	v_exp_f32_e64 v235, -v235
	v_exp_f32_e64 v236, -v236
	v_exp_f32_e64 v237, -v237
	v_exp_f32_e64 v238, -v238
	v_exp_f32_e64 v239, -v239
	v_exp_f32_e64 v240, -v240
	v_exp_f32_e64 v241, -v241
	v_exp_f32_e64 v106, -v106
	v_exp_f32_e64 v107, -v107
	v_exp_f32_e64 v108, -v108
	v_exp_f32_e64 v109, -v109
	v_exp_f32_e64 v110, -v110
	v_exp_f32_e64 v111, -v111
	v_exp_f32_e64 v112, -v112
	v_exp_f32_e64 v113, -v113
	s_nop 0
	v_mul_f32_e32 v50, v234, v50
	v_mul_f32_e32 v51, v235, v51
	v_mul_f32_e32 v52, v236, v52
	v_mul_f32_e32 v53, v237, v53
	v_mul_f32_e32 v54, v238, v54
	v_mul_f32_e32 v55, v239, v55
	v_mul_f32_e32 v56, v240, v56
	v_mul_f32_e32 v57, v241, v57
	v_mul_f32_e32 v58, v106, v58
	v_mul_f32_e32 v59, v107, v59
	v_mul_f32_e32 v60, v108, v60
	v_mul_f32_e32 v61, v109, v61
	v_mul_f32_e32 v62, v110, v62
	v_mul_f32_e32 v63, v111, v63
	v_mul_f32_e32 v64, v112, v64
	v_mul_f32_e32 v65, v113, v65
	v_mul_f32_e32 v216, v234, v216
	v_mul_f32_e32 v217, v235, v217
	v_mul_f32_e32 v214, v236, v214
	v_mul_f32_e32 v215, v237, v215
	v_mul_f32_e32 v212, v238, v212
	v_mul_f32_e32 v213, v239, v213
	v_mul_f32_e32 v210, v240, v210
	v_mul_f32_e32 v211, v241, v211
	v_mul_f32_e32 v208, v106, v208
	v_mul_f32_e32 v209, v107, v209
	v_mul_f32_e32 v204, v108, v204
	v_mul_f32_e32 v205, v109, v205
	v_mul_f32_e32 v202, v110, v202
	v_mul_f32_e32 v203, v111, v203
	v_mul_f32_e32 v196, v112, v196
	v_mul_f32_e32 v197, v113, v197
	s_nop 1
.Lm_norescale0:
	s_waitcnt lgkmcnt(3)
	v_mfma_f32_32x32x16_f16 v[74:89], v[154:157], v[70:73], v[74:89]
	ds_read_b128 v[154:157], v218 offset:1024
	v_exp_f32_e32 v234, v126
	v_exp_f32_e32 v235, v127
	v_exp_f32_e32 v236, v128
	v_exp_f32_e32 v237, v129
	v_exp_f32_e32 v238, v130
	v_exp_f32_e32 v239, v131
	v_exp_f32_e32 v240, v132
	v_exp_f32_e32 v241, v133
	s_waitcnt lgkmcnt(3)
	v_mfma_f32_32x32x16_f16 v[74:89], v[242:245], v[90:93], v[74:89]
	v_exp_f32_e32 v106, v134
	v_exp_f32_e32 v107, v135
	v_exp_f32_e32 v108, v136
	v_exp_f32_e32 v109, v137
	v_exp_f32_e32 v110, v138
	v_exp_f32_e32 v111, v139
	v_exp_f32_e32 v112, v140
	v_exp_f32_e32 v113, v141
	v_pk_add_f32 v[50:51], v[234:235], v[50:51]
	v_pk_add_f32 v[52:53], v[236:237], v[52:53]
	v_pk_add_f32 v[54:55], v[238:239], v[54:55]
	v_pk_add_f32 v[56:57], v[240:241], v[56:57]
	s_waitcnt lgkmcnt(2)
	v_mfma_f32_32x32x16_f16 v[74:89], v[246:249], v[94:97], v[74:89]
	s_setprio 1
	v_pk_add_f32 v[58:59], v[106:107], v[58:59]
	v_pk_add_f32 v[60:61], v[108:109], v[60:61]
	v_pk_add_f32 v[62:63], v[110:111], v[62:63]
	v_pk_add_f32 v[64:65], v[112:113], v[64:65]
	v_fma_mix_f32 v216, v234, v114, v216 op_sel:[0,0,0] op_sel_hi:[0,1,0]
	v_fma_mix_f32 v217, v235, v114, v217 op_sel:[0,1,0] op_sel_hi:[0,1,0]
	v_fma_mix_f32 v214, v236, v115, v214 op_sel:[0,0,0] op_sel_hi:[0,1,0]
	v_fma_mix_f32 v215, v237, v115, v215 op_sel:[0,1,0] op_sel_hi:[0,1,0]
	v_fma_mix_f32 v212, v238, v116, v212 op_sel:[0,0,0] op_sel_hi:[0,1,0]
	v_fma_mix_f32 v213, v239, v116, v213 op_sel:[0,1,0] op_sel_hi:[0,1,0]
	v_fma_mix_f32 v210, v240, v117, v210 op_sel:[0,0,0] op_sel_hi:[0,1,0]
	v_fma_mix_f32 v211, v241, v117, v211 op_sel:[0,1,0] op_sel_hi:[0,1,0]
	v_fma_mix_f32 v208, v106, v118, v208 op_sel:[0,0,0] op_sel_hi:[0,1,0]
	v_fma_mix_f32 v209, v107, v118, v209 op_sel:[0,1,0] op_sel_hi:[0,1,0]
	v_fma_mix_f32 v204, v108, v119, v204 op_sel:[0,0,0] op_sel_hi:[0,1,0]
	v_fma_mix_f32 v205, v109, v119, v205 op_sel:[0,1,0] op_sel_hi:[0,1,0]
	v_fma_mix_f32 v202, v110, v120, v202 op_sel:[0,0,0] op_sel_hi:[0,1,0]
	v_fma_mix_f32 v203, v111, v120, v203 op_sel:[0,1,0] op_sel_hi:[0,1,0]
	v_fma_mix_f32 v196, v112, v121, v196 op_sel:[0,0,0] op_sel_hi:[0,1,0]
	v_fma_mix_f32 v197, v113, v121, v197 op_sel:[0,1,0] op_sel_hi:[0,1,0]
	v_max3_f32 v254, v74, v75, v76
	v_max3_f32 v255, v77, v78, v79
	v_max3_f32 v254, v254, v80, v81
	v_max3_f32 v255, v255, v82, v83
	v_max3_f32 v254, v254, v84, v85
	v_max3_f32 v255, v255, v86, v87
	v_max3_f32 v254, v254, v88, v89
	v_max_f32_e32 v254, v254, v255
	v_cmp_lt_f32_e32 vcc, s5, v254
	s_cbranch_vccz .Lm_norescale1
	v_max_f32_e32 v234, 0, v74
	v_max_f32_e32 v235, 0, v75
	v_max_f32_e32 v236, 0, v76
	v_max_f32_e32 v237, 0, v77
	v_max_f32_e32 v238, 0, v78
	v_max_f32_e32 v239, 0, v79
	v_max_f32_e32 v240, 0, v80
	v_max_f32_e32 v241, 0, v81
	v_max_f32_e32 v106, 0, v82
	v_max_f32_e32 v107, 0, v83
	v_max_f32_e32 v108, 0, v84
	v_max_f32_e32 v109, 0, v85
	v_max_f32_e32 v110, 0, v86
	v_max_f32_e32 v111, 0, v87
	v_max_f32_e32 v112, 0, v88
	v_max_f32_e32 v113, 0, v89
	v_sub_f32_e32 v74, v74, v234
	v_sub_f32_e32 v75, v75, v235
	v_sub_f32_e32 v76, v76, v236
	v_sub_f32_e32 v77, v77, v237
	v_sub_f32_e32 v78, v78, v238
	v_sub_f32_e32 v79, v79, v239
	v_sub_f32_e32 v80, v80, v240
	v_sub_f32_e32 v81, v81, v241
	v_sub_f32_e32 v82, v82, v106
	v_sub_f32_e32 v83, v83, v107
	v_sub_f32_e32 v84, v84, v108
	v_sub_f32_e32 v85, v85, v109
	v_sub_f32_e32 v86, v86, v110
	v_sub_f32_e32 v87, v87, v111
	v_sub_f32_e32 v88, v88, v112
	v_sub_f32_e32 v89, v89, v113
	v_sub_f32_e32 v34, v34, v234
	v_sub_f32_e32 v35, v35, v235
	v_sub_f32_e32 v36, v36, v236
	v_sub_f32_e32 v37, v37, v237
	v_sub_f32_e32 v38, v38, v238
	v_sub_f32_e32 v39, v39, v239
	v_sub_f32_e32 v40, v40, v240
	v_sub_f32_e32 v41, v41, v241
	v_sub_f32_e32 v42, v42, v106
	v_sub_f32_e32 v43, v43, v107
	v_sub_f32_e32 v44, v44, v108
	v_sub_f32_e32 v45, v45, v109
	v_sub_f32_e32 v46, v46, v110
	v_sub_f32_e32 v47, v47, v111
	v_sub_f32_e32 v48, v48, v112
	v_sub_f32_e32 v49, v49, v113
	v_exp_f32_e64 v234, -v234
	v_exp_f32_e64 v235, -v235
	v_exp_f32_e64 v236, -v236
	v_exp_f32_e64 v237, -v237
	v_exp_f32_e64 v238, -v238
	v_exp_f32_e64 v239, -v239
	v_exp_f32_e64 v240, -v240
	v_exp_f32_e64 v241, -v241
	v_exp_f32_e64 v106, -v106
	v_exp_f32_e64 v107, -v107
	v_exp_f32_e64 v108, -v108
	v_exp_f32_e64 v109, -v109
	v_exp_f32_e64 v110, -v110
	v_exp_f32_e64 v111, -v111
	v_exp_f32_e64 v112, -v112
	v_exp_f32_e64 v113, -v113
	s_nop 0
	v_mul_f32_e32 v18, v234, v18
	v_mul_f32_e32 v19, v235, v19
	v_mul_f32_e32 v20, v236, v20
	v_mul_f32_e32 v21, v237, v21
	v_mul_f32_e32 v22, v238, v22
	v_mul_f32_e32 v23, v239, v23
	v_mul_f32_e32 v24, v240, v24
	v_mul_f32_e32 v25, v241, v25
	v_mul_f32_e32 v26, v106, v26
	v_mul_f32_e32 v27, v107, v27
	v_mul_f32_e32 v28, v108, v28
	v_mul_f32_e32 v29, v109, v29
	v_mul_f32_e32 v30, v110, v30
	v_mul_f32_e32 v31, v111, v31
	v_mul_f32_e32 v32, v112, v32
	v_mul_f32_e32 v33, v113, v33
	v_mul_f32_e32 v206, v234, v206
	v_mul_f32_e32 v207, v235, v207
	v_mul_f32_e32 v200, v236, v200
	v_mul_f32_e32 v201, v237, v201
	v_mul_f32_e32 v198, v238, v198
	v_mul_f32_e32 v199, v239, v199
	v_mul_f32_e32 v194, v240, v194
	v_mul_f32_e32 v195, v241, v195
	v_mul_f32_e32 v192, v106, v192
	v_mul_f32_e32 v193, v107, v193
	v_mul_f32_e32 v190, v108, v190
	v_mul_f32_e32 v191, v109, v191
	v_mul_f32_e32 v188, v110, v188
	v_mul_f32_e32 v189, v111, v189
	v_mul_f32_e32 v186, v112, v186
	v_mul_f32_e32 v187, v113, v187
	s_nop 1
